# barrier 9 split with single-lane ready-counter add and single-lane wait polls (barrier 4 wait also single lane)
# speedup vs baseline: 1.0137x; 1.0137x over previous
.LBB0_817:
	v_add_u32_e32 v12, s6, v222
	v_ashrrev_i32_e32 v13, 31, v12
	v_lshlrev_b64 v[12:13], 11, v[12:13]
	v_lshl_add_u64 v[56:57], v[4:5], 0, v[12:13]
	v_add_co_u32_e32 v58, vcc, 0x8000, v56
	global_load_dwordx4 v[12:15], v[56:57], off
	global_load_dwordx4 v[16:19], v[2:3], off
	v_addc_co_u32_e32 v59, vcc, 0, v57, vcc
	v_add_co_u32_e32 v60, vcc, 0x10000, v56
	global_load_dwordx4 v[20:23], v[58:59], off
	s_nop 0
	v_addc_co_u32_e32 v61, vcc, 0, v57, vcc
	v_add_co_u32_e32 v62, vcc, 0x18000, v56
	global_load_dwordx4 v[24:27], v[60:61], off
	s_nop 0
	v_addc_co_u32_e32 v63, vcc, 0, v57, vcc
	global_load_dwordx4 v[28:31], v[62:63], off
	global_load_dwordx4 v[32:35], v[56:57], off offset:64
	global_load_dwordx4 v[36:39], v[2:3], off offset:64
	global_load_dwordx4 v[40:43], v[58:59], off offset:64
	global_load_dwordx4 v[44:47], v[60:61], off offset:64
	global_load_dwordx4 v[48:51], v[62:63], off offset:64
	s_and_b64 vcc, exec, s[4:5]
	s_waitcnt vmcnt(8)
	v_mfma_f32_16x16x32_bf16 v[12:15], v[12:15], v[16:19], 0
	s_waitcnt vmcnt(7)
	v_mfma_f32_16x16x32_bf16 v[20:23], v[20:23], v[16:19], 0
	s_waitcnt vmcnt(6)
	v_mfma_f32_16x16x32_bf16 v[24:27], v[24:27], v[16:19], 0
	s_waitcnt vmcnt(5)
	v_mfma_f32_16x16x32_bf16 v[16:19], v[28:31], v[16:19], 0
	global_load_dwordx4 v[28:31], v[56:57], off offset:128
	global_load_dwordx4 v[52:55], v[2:3], off offset:128
	s_waitcnt vmcnt(5)
	v_mfma_f32_16x16x32_bf16 v[12:15], v[32:35], v[36:39], v[12:15]
	global_load_dwordx4 v[32:35], v[58:59], off offset:128
	s_waitcnt vmcnt(5)
	v_mfma_f32_16x16x32_bf16 v[20:23], v[40:43], v[36:39], v[20:23]
	global_load_dwordx4 v[40:43], v[60:61], off offset:128
	s_waitcnt vmcnt(5)
	v_mfma_f32_16x16x32_bf16 v[24:27], v[44:47], v[36:39], v[24:27]
	global_load_dwordx4 v[44:47], v[62:63], off offset:128
	s_waitcnt vmcnt(5)
	v_mfma_f32_16x16x32_bf16 v[16:19], v[48:51], v[36:39], v[16:19]
	global_load_dwordx4 v[36:39], v[56:57], off offset:192
	global_load_dwordx4 v[48:51], v[2:3], off offset:192
	s_waitcnt vmcnt(5)
	v_mfma_f32_16x16x32_bf16 v[12:15], v[28:31], v[52:55], v[12:15]
	global_load_dwordx4 v[28:31], v[58:59], off offset:192
	s_waitcnt vmcnt(5)
	v_mfma_f32_16x16x32_bf16 v[20:23], v[32:35], v[52:55], v[20:23]
	global_load_dwordx4 v[32:35], v[60:61], off offset:192
	s_waitcnt vmcnt(5)
	v_mfma_f32_16x16x32_bf16 v[24:27], v[40:43], v[52:55], v[24:27]
	global_load_dwordx4 v[40:43], v[62:63], off offset:192
	s_barrier
	s_waitcnt vmcnt(5)
	v_mfma_f32_16x16x32_bf16 v[16:19], v[44:47], v[52:55], v[16:19]
	s_waitcnt vmcnt(3)
	v_mfma_f32_16x16x32_bf16 v[12:15], v[36:39], v[48:51], v[12:15]
	s_waitcnt vmcnt(2)
	v_mfma_f32_16x16x32_bf16 v[20:23], v[28:31], v[48:51], v[20:23]
	s_waitcnt vmcnt(1)
	v_mfma_f32_16x16x32_bf16 v[24:27], v[32:35], v[48:51], v[24:27]
	s_waitcnt vmcnt(0)
	v_mfma_f32_16x16x32_bf16 v[16:19], v[40:43], v[48:51], v[16:19]
	s_nop 1
	ds_write_b128 v11, v[12:15]
	s_nop 0
	ds_write_b128 v11, v[20:23] offset:1024
	s_nop 0
	ds_write_b128 v11, v[24:27] offset:2048
	s_nop 0
	ds_write_b128 v11, v[16:19] offset:3072
	s_waitcnt lgkmcnt(0)
	s_barrier
	s_cbranch_vccnz .LBB0_816
	v_add_u32_e32 v80, s6, v10
	v_ashrrev_i32_e32 v81, 31, v80
	v_lshl_add_u64 v[82:83], v[80:81], 2, v[6:7]
	global_load_dwordx4 v[12:15], v[82:83], off
	global_load_dwordx4 v[88:91], v[82:83], off offset:64
	global_load_dwordx4 v[92:95], v[82:83], off offset:128
	global_load_dwordx4 v[96:99], v[82:83], off offset:192
	ds_read_b128 v[16:19], v1
	ds_read_b128 v[20:23], v1 offset:1024
	ds_read_b128 v[24:27], v1 offset:4096
	ds_read_b128 v[28:31], v1 offset:5120
	ds_read_b128 v[32:35], v1 offset:8192
	ds_read_b128 v[36:39], v1 offset:9216
	ds_read_b128 v[40:43], v1 offset:12288
	ds_read_b128 v[44:47], v1 offset:13312
	ds_read_b128 v[48:51], v1 offset:16384
	ds_read_b128 v[52:55], v1 offset:17408
	ds_read_b128 v[56:59], v1 offset:20480
	ds_read_b128 v[60:63], v1 offset:21504
	ds_read_b128 v[64:67], v1 offset:24576
	ds_read_b128 v[68:71], v1 offset:25600
	ds_read_b128 v[72:75], v1 offset:28672
	ds_read_b128 v[76:79], v1 offset:29696
	s_waitcnt lgkmcnt(13)
	v_pk_add_f32 v[18:19], v[18:19], v[26:27]
	v_pk_add_f32 v[16:17], v[16:17], v[24:25]
	s_waitcnt lgkmcnt(11)
	v_pk_add_f32 v[18:19], v[18:19], v[34:35]
	v_pk_add_f32 v[16:17], v[16:17], v[32:33]
	s_waitcnt lgkmcnt(9)
	v_pk_add_f32 v[18:19], v[18:19], v[42:43]
	v_pk_add_f32 v[16:17], v[16:17], v[40:41]
	s_waitcnt lgkmcnt(7)
	v_pk_add_f32 v[18:19], v[18:19], v[50:51]
	v_pk_add_f32 v[16:17], v[16:17], v[48:49]
	s_waitcnt lgkmcnt(5)
	v_pk_add_f32 v[18:19], v[18:19], v[58:59]
	v_pk_add_f32 v[16:17], v[16:17], v[56:57]
	s_waitcnt lgkmcnt(3)
	v_pk_add_f32 v[18:19], v[18:19], v[66:67]
	v_pk_add_f32 v[16:17], v[16:17], v[64:65]
	s_waitcnt lgkmcnt(1)
	v_pk_add_f32 v[18:19], v[18:19], v[74:75]
	v_pk_add_f32 v[16:17], v[16:17], v[72:73]
	v_lshl_add_u64 v[84:85], v[80:81], 1, v[8:9]
	v_pk_add_f32 v[20:21], v[20:21], v[28:29]
	s_waitcnt vmcnt(3)
	v_pk_add_f32 v[14:15], v[18:19], v[14:15]
	v_pk_add_f32 v[12:13], v[16:17], v[12:13]
	v_bfe_u32 v18, v14, 16, 1
	v_bfe_u32 v16, v12, 16, 1
	v_bfe_u32 v17, v13, 16, 1
	v_bfe_u32 v19, v15, 16, 1
	v_add3_u32 v12, v12, v16, s8
	v_add3_u32 v14, v14, v18, s8
	v_add3_u32 v13, v13, v17, s8
	v_add3_u32 v15, v15, v19, s8
	v_lshrrev_b32_e32 v12, 16, v12
	v_lshrrev_b32_e32 v14, 16, v14
	v_and_or_b32 v12, v13, s9, v12
	v_and_or_b32 v13, v15, s9, v14
	s_mov_b64 exec, 1
	v_mov_b32_e32 v24, 0x22160
	ds_read_b32 v25, v24
	v_mov_b32_e32 v26, s99
	v_lshrrev_b32_e32 v27, 16, v26
	v_mov_b32_e32 v32, s98
	v_min_u32_e32 v32, 8, v32
	v_mov_b32_e32 v33, 0
	s_waitcnt lgkmcnt(0)
	v_mul_lo_u32 v32, v32, v25

.Lgw_end_4:
	s_mov_b64 exec, -1
	global_store_dwordx2 v[84:85], v[12:13], off sc1
	v_pk_add_f32 v[18:19], v[22:23], v[30:31]
	v_pk_add_f32 v[20:21], v[20:21], v[36:37]
	v_pk_add_f32 v[18:19], v[18:19], v[38:39]
	v_pk_add_f32 v[20:21], v[20:21], v[44:45]
	v_pk_add_f32 v[18:19], v[18:19], v[46:47]
	v_pk_add_f32 v[20:21], v[20:21], v[52:53]
	v_pk_add_f32 v[18:19], v[18:19], v[54:55]
	v_pk_add_f32 v[20:21], v[20:21], v[60:61]
	v_pk_add_f32 v[18:19], v[18:19], v[62:63]
	v_pk_add_f32 v[20:21], v[20:21], v[68:69]
	v_pk_add_f32 v[18:19], v[18:19], v[70:71]
	s_waitcnt lgkmcnt(0)
	v_pk_add_f32 v[20:21], v[20:21], v[76:77]
	v_pk_add_f32 v[18:19], v[18:19], v[78:79]
	v_add_u32_e32 v16, 16, v80
	v_ashrrev_i32_e32 v17, 31, v16
	v_lshl_add_u64 v[16:17], v[16:17], 1, v[8:9]
	v_add_u32_e32 v84, 32, v80
	v_ashrrev_i32_e32 v85, 31, v84
	v_lshl_add_u64 v[84:85], v[84:85], 1, v[8:9]
	s_waitcnt vmcnt(3)
	v_pk_add_f32 v[14:15], v[18:19], v[90:91]
	v_pk_add_f32 v[12:13], v[20:21], v[88:89]
	v_bfe_u32 v20, v14, 16, 1
	v_bfe_u32 v18, v12, 16, 1
	v_bfe_u32 v19, v13, 16, 1
	v_bfe_u32 v21, v15, 16, 1
	v_add3_u32 v12, v12, v18, s8
	v_add3_u32 v14, v14, v20, s8
	v_add3_u32 v13, v13, v19, s8
	v_add3_u32 v15, v15, v21, s8
	v_lshrrev_b32_e32 v12, 16, v12
	v_lshrrev_b32_e32 v14, 16, v14
	v_and_or_b32 v12, v13, s9, v12
	v_and_or_b32 v13, v15, s9, v14
	global_store_dwordx2 v[16:17], v[12:13], off sc1
	ds_read_b128 v[16:19], v1 offset:2048
	ds_read_b128 v[20:23], v1 offset:3072
	ds_read_b128 v[24:27], v1 offset:6144
	ds_read_b128 v[28:31], v1 offset:7168
	ds_read_b128 v[32:35], v1 offset:10240
	ds_read_b128 v[36:39], v1 offset:11264
	ds_read_b128 v[40:43], v1 offset:14336
	ds_read_b128 v[44:47], v1 offset:15360
	ds_read_b128 v[48:51], v1 offset:18432
	ds_read_b128 v[52:55], v1 offset:19456
	ds_read_b128 v[56:59], v1 offset:22528
	ds_read_b128 v[60:63], v1 offset:23552
	ds_read_b128 v[64:67], v1 offset:26624
	ds_read_b128 v[68:71], v1 offset:27648
	ds_read_b128 v[72:75], v1 offset:30720
	ds_read_b128 v[76:79], v1 offset:31744
	s_waitcnt lgkmcnt(13)
	v_pk_add_f32 v[18:19], v[18:19], v[26:27]
	v_pk_add_f32 v[16:17], v[16:17], v[24:25]
	s_waitcnt lgkmcnt(11)
	v_pk_add_f32 v[18:19], v[18:19], v[34:35]
	v_pk_add_f32 v[16:17], v[16:17], v[32:33]
	s_waitcnt lgkmcnt(9)
	v_pk_add_f32 v[18:19], v[18:19], v[42:43]
	v_pk_add_f32 v[16:17], v[16:17], v[40:41]
	s_waitcnt lgkmcnt(7)
	v_pk_add_f32 v[18:19], v[18:19], v[50:51]
	v_pk_add_f32 v[16:17], v[16:17], v[48:49]
	s_waitcnt lgkmcnt(5)
	v_pk_add_f32 v[18:19], v[18:19], v[58:59]
	v_pk_add_f32 v[16:17], v[16:17], v[56:57]
	s_waitcnt lgkmcnt(3)
	v_pk_add_f32 v[18:19], v[18:19], v[66:67]
	v_pk_add_f32 v[16:17], v[16:17], v[64:65]
	s_waitcnt lgkmcnt(1)
	v_pk_add_f32 v[18:19], v[18:19], v[74:75]
	v_pk_add_f32 v[16:17], v[16:17], v[72:73]
	v_pk_add_f32 v[20:21], v[20:21], v[28:29]
	s_waitcnt vmcnt(3)
	v_pk_add_f32 v[14:15], v[18:19], v[94:95]
	v_pk_add_f32 v[12:13], v[16:17], v[92:93]
	v_bfe_u32 v18, v14, 16, 1
	v_bfe_u32 v16, v12, 16, 1
	v_bfe_u32 v17, v13, 16, 1
	v_bfe_u32 v19, v15, 16, 1
	v_add3_u32 v12, v12, v16, s8
	v_add3_u32 v14, v14, v18, s8
	v_add3_u32 v13, v13, v17, s8
	v_add3_u32 v15, v15, v19, s8
	v_lshrrev_b32_e32 v12, 16, v12
	v_lshrrev_b32_e32 v14, 16, v14
	v_and_or_b32 v12, v13, s9, v12
	v_and_or_b32 v13, v15, s9, v14
	global_store_dwordx2 v[84:85], v[12:13], off sc1
	v_pk_add_f32 v[18:19], v[22:23], v[30:31]
	v_pk_add_f32 v[20:21], v[20:21], v[36:37]
	v_pk_add_f32 v[18:19], v[18:19], v[38:39]
	v_pk_add_f32 v[20:21], v[20:21], v[44:45]
	v_pk_add_f32 v[18:19], v[18:19], v[46:47]
	v_pk_add_f32 v[20:21], v[20:21], v[52:53]
	v_pk_add_f32 v[18:19], v[18:19], v[54:55]
	v_pk_add_f32 v[20:21], v[20:21], v[60:61]
	v_pk_add_f32 v[18:19], v[18:19], v[62:63]
	v_pk_add_f32 v[20:21], v[20:21], v[68:69]
	v_pk_add_f32 v[18:19], v[18:19], v[70:71]
	s_waitcnt lgkmcnt(0)
	v_pk_add_f32 v[20:21], v[20:21], v[76:77]
	v_pk_add_f32 v[18:19], v[18:19], v[78:79]
	v_add_u32_e32 v16, 48, v80
	v_ashrrev_i32_e32 v17, 31, v16
	s_waitcnt vmcnt(3)
	v_pk_add_f32 v[14:15], v[18:19], v[98:99]
	v_pk_add_f32 v[12:13], v[20:21], v[96:97]
	v_bfe_u32 v20, v14, 16, 1
	v_bfe_u32 v18, v12, 16, 1
	v_bfe_u32 v19, v13, 16, 1
	v_bfe_u32 v21, v15, 16, 1
	v_add3_u32 v12, v12, v18, s8
	v_add3_u32 v14, v14, v20, s8
	v_add3_u32 v13, v13, v19, s8
	v_add3_u32 v15, v15, v21, s8
	v_lshrrev_b32_e32 v12, 16, v12
	v_lshrrev_b32_e32 v14, 16, v14
	v_and_or_b32 v12, v13, s9, v12
	v_and_or_b32 v13, v15, s9, v14
	v_lshl_add_u64 v[14:15], v[16:17], 1, v[8:9]
	global_store_dwordx2 v[14:15], v[12:13], off sc1
	s_branch .LBB0_816

.LBB0_1371:
	s_or_b64 exec, exec, s[4:5]
	s_waitcnt lgkmcnt(0)
	s_barrier
	s_and_saveexec_b64 s[4:5], s[6:7]
	s_cbranch_execz .LBB0_1373
	v_lshl_add_u32 v1, v0, 2, 0
	ds_read_b32 v1, v1 offset:128
	v_lshl_or_b32 v2, s18, 5, v0
	v_readlane_b32 s36, v253, 46
	v_ashrrev_i32_e32 v3, 31, v2
	v_readlane_b32 s50, v253, 60
	v_readlane_b32 s51, v253, 61
	s_waitcnt lgkmcnt(0)
	v_min_i32_e32 v1, v1, v252
	v_and_b32_e32 v1, -2, v1
	v_lshl_add_u64 v[2:3], v[2:3], 2, s[50:51]
	v_add_co_u32_e32 v2, vcc, 0x1582000, v2
	v_readlane_b32 s37, v253, 47
	s_nop 0
	v_addc_co_u32_e32 v3, vcc, 0, v3, vcc
	v_readlane_b32 s38, v253, 48
	v_readlane_b32 s39, v253, 49
	v_readlane_b32 s40, v253, 50
	v_readlane_b32 s41, v253, 51
	v_readlane_b32 s42, v253, 52
	v_readlane_b32 s43, v253, 53
	v_readlane_b32 s44, v253, 54
	v_readlane_b32 s45, v253, 55
	v_readlane_b32 s46, v253, 56
	v_readlane_b32 s47, v253, 57
	v_readlane_b32 s48, v253, 58
	v_readlane_b32 s49, v253, 59
	global_store_dword v[2:3], v1, off sc1
	s_waitcnt vmcnt(0)
	s_mov_b64 exec, 1
	v_mov_b32_e32 v2, 0
	v_mov_b32_e32 v3, 1
	global_atomic_add v2, v3, s[100:101] offset:128

.Lgb_chk_9:
	v_mov_b32_e32 v6, 0x80
	v_mov_b32_e32 v9, 32
	v_cmp_ge_u32_e32 vcc, v11, v9
	s_cbranch_vccnz .Lgb_done_9

.LBB0_1687:
	s_or_b64 exec, exec, s[6:7]
	v_add_u32_e32 v1, s30, v2
	ds_write_b32 v1, v3 offset:4
	v_add_u32_e32 v1, s30, v250
	s_waitcnt lgkmcnt(0)
	s_barrier
	ds_read_b128 v[8:11], v1
	v_cmp_eq_u32_e32 vcc, 0, v192
	s_waitcnt lgkmcnt(0)
	s_barrier
	v_and_b32_e32 v17, 0x80, v0
	v_and_b32_e32 v205, 31, v0
	s_waitcnt lgkmcnt(0)
	v_max_i32_e32 v2, v8, v9
	v_min_i32_e32 v6, v10, v11
	v_min_i32_e32 v3, v8, v9
	v_max_i32_e32 v5, v10, v11
	v_max_i32_e32 v8, v2, v6
	v_min_i32_e32 v2, v2, v6
	v_cndmask_b32_e32 v6, v2, v8, vcc
	v_cndmask_b32_e32 v2, v8, v2, vcc
	v_max_i32_e32 v8, v3, v5
	v_min_i32_e32 v3, v3, v5
	v_cndmask_b32_e32 v5, v3, v8, vcc
	v_cndmask_b32_e32 v3, v8, v3, vcc
	v_max_i32_e32 v8, v6, v5
	v_min_i32_e32 v5, v6, v5
	v_cndmask_b32_e32 v6, v5, v8, vcc
	v_cndmask_b32_e32 v5, v8, v5, vcc
	v_max_i32_e32 v9, v2, v3
	v_min_i32_e32 v3, v2, v3
	v_xor_b32_e32 v2, 1, v7
	v_add_u32_e32 v8, 64, v4
	v_cmp_lt_i32_e64 s[6:7], v2, v8
	v_cndmask_b32_e32 v10, v3, v9, vcc
	v_cndmask_b32_e32 v3, v9, v3, vcc
	v_cndmask_b32_e64 v2, v7, v2, s[6:7]
	v_lshlrev_b32_e32 v2, 2, v2
	ds_bpermute_b32 v4, v2, v6
	ds_bpermute_b32 v12, v2, v5
	v_and_b32_e32 v9, 2, v0
	v_cmp_ne_u32_e64 s[6:7], 0, v9
	s_xor_b64 s[6:7], vcc, s[6:7]
	s_waitcnt lgkmcnt(1)
	v_max_i32_e32 v11, v6, v4
	v_min_i32_e32 v4, v6, v4
	v_cndmask_b32_e64 v4, v4, v11, s[6:7]
	ds_bpermute_b32 v6, v2, v10
	s_waitcnt lgkmcnt(1)
	v_max_i32_e32 v11, v5, v12
	v_min_i32_e32 v5, v5, v12
	ds_bpermute_b32 v12, v2, v3
	v_cndmask_b32_e64 v5, v5, v11, s[6:7]
	s_waitcnt lgkmcnt(1)
	v_max_i32_e32 v11, v10, v6
	v_min_i32_e32 v6, v10, v6
	v_cndmask_b32_e64 v6, v6, v11, s[6:7]
	s_waitcnt lgkmcnt(0)
	v_max_i32_e32 v10, v3, v12
	v_min_i32_e32 v3, v3, v12
	v_cndmask_b32_e64 v3, v3, v10, s[6:7]
	v_max_i32_e32 v10, v4, v6
	v_min_i32_e32 v4, v4, v6
	v_cmp_eq_u32_e64 s[6:7], 0, v9
	v_max_i32_e32 v9, v5, v3
	v_min_i32_e32 v3, v5, v3
	v_cndmask_b32_e64 v6, v4, v10, s[6:7]
	v_cndmask_b32_e64 v5, v3, v9, s[6:7]
	v_cndmask_b32_e64 v4, v10, v4, s[6:7]
	v_cndmask_b32_e64 v3, v9, v3, s[6:7]
	v_max_i32_e32 v9, v6, v5
	v_min_i32_e32 v5, v6, v5
	v_cndmask_b32_e64 v6, v5, v9, s[6:7]
	v_cndmask_b32_e64 v5, v9, v5, s[6:7]
	v_max_i32_e32 v9, v4, v3
	v_min_i32_e32 v4, v4, v3
	v_xor_b32_e32 v3, 2, v7
	v_cmp_lt_i32_e64 s[8:9], v3, v8
	v_cndmask_b32_e64 v11, v4, v9, s[6:7]
	v_cndmask_b32_e64 v4, v9, v4, s[6:7]
	v_cndmask_b32_e64 v3, v7, v3, s[8:9]
	v_lshlrev_b32_e32 v3, 2, v3
	ds_bpermute_b32 v10, v3, v6
	ds_bpermute_b32 v13, v3, v5
	v_and_b32_e32 v9, 4, v0
	v_cmp_ne_u32_e64 s[8:9], 0, v9
	s_xor_b64 s[10:11], s[6:7], s[8:9]
	s_waitcnt lgkmcnt(1)
	v_max_i32_e32 v12, v6, v10
	v_min_i32_e32 v6, v6, v10
	v_cndmask_b32_e64 v6, v6, v12, s[10:11]
	ds_bpermute_b32 v10, v3, v11
	s_waitcnt lgkmcnt(1)
	v_max_i32_e32 v12, v5, v13
	v_min_i32_e32 v5, v5, v13
	v_cndmask_b32_e64 v5, v5, v12, s[10:11]
	ds_bpermute_b32 v12, v3, v4
	s_waitcnt lgkmcnt(1)
	v_max_i32_e32 v13, v11, v10
	v_min_i32_e32 v10, v11, v10
	ds_bpermute_b32 v11, v2, v6
	v_cndmask_b32_e64 v10, v10, v13, s[10:11]
	s_waitcnt lgkmcnt(1)
	v_max_i32_e32 v13, v4, v12
	v_min_i32_e32 v4, v4, v12
	v_cndmask_b32_e64 v4, v4, v13, s[10:11]
	ds_bpermute_b32 v13, v2, v5
	s_waitcnt lgkmcnt(1)
	v_max_i32_e32 v12, v6, v11
	v_min_i32_e32 v6, v6, v11
	s_xor_b64 s[8:9], vcc, s[8:9]
	v_cndmask_b32_e64 v6, v6, v12, s[8:9]
	ds_bpermute_b32 v11, v2, v10
	s_waitcnt lgkmcnt(1)
	v_max_i32_e32 v12, v5, v13
	v_min_i32_e32 v5, v5, v13
	ds_bpermute_b32 v13, v2, v4
	v_cndmask_b32_e64 v5, v5, v12, s[8:9]
	s_waitcnt lgkmcnt(1)
	v_max_i32_e32 v12, v10, v11
	v_min_i32_e32 v10, v10, v11
	v_cndmask_b32_e64 v10, v10, v12, s[8:9]
	s_waitcnt lgkmcnt(0)
	v_max_i32_e32 v11, v4, v13
	v_min_i32_e32 v4, v4, v13
	v_cndmask_b32_e64 v4, v4, v11, s[8:9]
	v_max_i32_e32 v11, v6, v10
	v_min_i32_e32 v6, v6, v10
	v_cmp_eq_u32_e64 s[8:9], 0, v9
	v_max_i32_e32 v10, v5, v4
	v_min_i32_e32 v4, v5, v4
	v_cndmask_b32_e64 v9, v6, v11, s[8:9]
	v_cndmask_b32_e64 v5, v4, v10, s[8:9]
	v_cndmask_b32_e64 v6, v11, v6, s[8:9]
	v_cndmask_b32_e64 v4, v10, v4, s[8:9]
	v_max_i32_e32 v10, v9, v5
	v_min_i32_e32 v5, v9, v5
	v_cndmask_b32_e64 v9, v5, v10, s[8:9]
	v_cndmask_b32_e64 v5, v10, v5, s[8:9]
	v_max_i32_e32 v10, v6, v4
	v_min_i32_e32 v6, v6, v4
	v_xor_b32_e32 v4, 4, v7
	v_cmp_lt_i32_e64 s[10:11], v4, v8
	v_cndmask_b32_e64 v12, v6, v10, s[8:9]
	v_cndmask_b32_e64 v6, v10, v6, s[8:9]
	v_cndmask_b32_e64 v4, v7, v4, s[10:11]
	v_lshlrev_b32_e32 v4, 2, v4
	ds_bpermute_b32 v11, v4, v9
	ds_bpermute_b32 v14, v4, v5
	v_and_b32_e32 v10, 8, v0
	v_cmp_ne_u32_e64 s[10:11], 0, v10
	s_xor_b64 s[12:13], s[8:9], s[10:11]
	s_waitcnt lgkmcnt(1)
	v_max_i32_e32 v13, v9, v11
	v_min_i32_e32 v9, v9, v11
	v_cndmask_b32_e64 v9, v9, v13, s[12:13]
	ds_bpermute_b32 v11, v4, v12
	s_waitcnt lgkmcnt(1)
	v_max_i32_e32 v13, v5, v14
	v_min_i32_e32 v5, v5, v14
	v_cndmask_b32_e64 v5, v5, v13, s[12:13]
	ds_bpermute_b32 v13, v4, v6
	s_waitcnt lgkmcnt(1)
	v_max_i32_e32 v14, v12, v11
	v_min_i32_e32 v11, v12, v11
	ds_bpermute_b32 v12, v3, v9
	v_cndmask_b32_e64 v11, v11, v14, s[12:13]
	s_waitcnt lgkmcnt(1)
	v_max_i32_e32 v14, v6, v13
	v_min_i32_e32 v6, v6, v13
	v_cndmask_b32_e64 v6, v6, v14, s[12:13]
	ds_bpermute_b32 v14, v3, v5
	s_waitcnt lgkmcnt(1)
	v_max_i32_e32 v13, v9, v12
	v_min_i32_e32 v9, v9, v12
	s_xor_b64 s[12:13], s[6:7], s[10:11]
	v_cndmask_b32_e64 v9, v9, v13, s[12:13]
	ds_bpermute_b32 v12, v3, v11
	s_waitcnt lgkmcnt(1)
	v_max_i32_e32 v13, v5, v14
	v_min_i32_e32 v5, v5, v14
	v_cndmask_b32_e64 v5, v5, v13, s[12:13]
	ds_bpermute_b32 v13, v3, v6
	s_waitcnt lgkmcnt(1)
	v_max_i32_e32 v14, v11, v12
	v_min_i32_e32 v11, v11, v12
	ds_bpermute_b32 v12, v2, v9
	v_cndmask_b32_e64 v11, v11, v14, s[12:13]
	s_waitcnt lgkmcnt(1)
	v_max_i32_e32 v14, v6, v13
	v_min_i32_e32 v6, v6, v13
	v_cndmask_b32_e64 v6, v6, v14, s[12:13]
	ds_bpermute_b32 v14, v2, v5
	s_waitcnt lgkmcnt(1)
	v_max_i32_e32 v13, v9, v12
	v_min_i32_e32 v9, v9, v12
	s_xor_b64 s[10:11], vcc, s[10:11]
	v_cndmask_b32_e64 v9, v9, v13, s[10:11]
	ds_bpermute_b32 v12, v2, v11
	s_waitcnt lgkmcnt(1)
	v_max_i32_e32 v13, v5, v14
	v_min_i32_e32 v5, v5, v14
	ds_bpermute_b32 v14, v2, v6
	v_cndmask_b32_e64 v5, v5, v13, s[10:11]
	s_waitcnt lgkmcnt(1)
	v_max_i32_e32 v13, v11, v12
	v_min_i32_e32 v11, v11, v12
	v_cndmask_b32_e64 v11, v11, v13, s[10:11]
	s_waitcnt lgkmcnt(0)
	v_max_i32_e32 v12, v6, v14
	v_min_i32_e32 v6, v6, v14
	v_cndmask_b32_e64 v6, v6, v12, s[10:11]
	v_max_i32_e32 v12, v9, v11
	v_min_i32_e32 v9, v9, v11
	v_cmp_eq_u32_e64 s[10:11], 0, v10
	v_max_i32_e32 v11, v5, v6
	v_min_i32_e32 v5, v5, v6
	v_cndmask_b32_e64 v10, v9, v12, s[10:11]
	v_cndmask_b32_e64 v6, v5, v11, s[10:11]
	v_cndmask_b32_e64 v9, v12, v9, s[10:11]
	v_cndmask_b32_e64 v5, v11, v5, s[10:11]
	v_max_i32_e32 v11, v10, v6
	v_min_i32_e32 v6, v10, v6
	v_cndmask_b32_e64 v10, v6, v11, s[10:11]
	v_cndmask_b32_e64 v6, v11, v6, s[10:11]
	v_max_i32_e32 v11, v9, v5
	v_min_i32_e32 v9, v9, v5
	v_xor_b32_e32 v5, 8, v7
	v_cmp_lt_i32_e64 s[12:13], v5, v8
	v_cndmask_b32_e64 v13, v9, v11, s[10:11]
	v_cndmask_b32_e64 v9, v11, v9, s[10:11]
	v_cndmask_b32_e64 v5, v7, v5, s[12:13]
	v_lshlrev_b32_e32 v5, 2, v5
	ds_bpermute_b32 v12, v5, v10
	ds_bpermute_b32 v15, v5, v6
	v_and_b32_e32 v11, 16, v0
	v_cmp_ne_u32_e64 s[12:13], 0, v11
	s_xor_b64 s[14:15], s[10:11], s[12:13]
	s_waitcnt lgkmcnt(1)
	v_max_i32_e32 v14, v10, v12
	v_min_i32_e32 v10, v10, v12
	v_cndmask_b32_e64 v10, v10, v14, s[14:15]
	ds_bpermute_b32 v12, v5, v13
	s_waitcnt lgkmcnt(1)
	v_max_i32_e32 v14, v6, v15
	v_min_i32_e32 v6, v6, v15
	v_cndmask_b32_e64 v6, v6, v14, s[14:15]
	ds_bpermute_b32 v14, v5, v9
	s_waitcnt lgkmcnt(1)
	v_max_i32_e32 v15, v13, v12
	v_min_i32_e32 v12, v13, v12
	ds_bpermute_b32 v13, v4, v10
	v_cndmask_b32_e64 v12, v12, v15, s[14:15]
	s_waitcnt lgkmcnt(1)
	v_max_i32_e32 v15, v9, v14
	v_min_i32_e32 v9, v9, v14
	v_cndmask_b32_e64 v9, v9, v15, s[14:15]
	ds_bpermute_b32 v15, v4, v6
	s_waitcnt lgkmcnt(1)
	v_max_i32_e32 v14, v10, v13
	v_min_i32_e32 v10, v10, v13
	s_xor_b64 s[14:15], s[8:9], s[12:13]
	v_cndmask_b32_e64 v10, v10, v14, s[14:15]
	ds_bpermute_b32 v13, v4, v12
	s_waitcnt lgkmcnt(1)
	v_max_i32_e32 v14, v6, v15
	v_min_i32_e32 v6, v6, v15
	v_cndmask_b32_e64 v6, v6, v14, s[14:15]
	ds_bpermute_b32 v14, v4, v9
	s_waitcnt lgkmcnt(1)
	v_max_i32_e32 v15, v12, v13
	v_min_i32_e32 v12, v12, v13
	ds_bpermute_b32 v13, v3, v10
	v_cndmask_b32_e64 v12, v12, v15, s[14:15]
	s_waitcnt lgkmcnt(1)
	v_max_i32_e32 v15, v9, v14
	v_min_i32_e32 v9, v9, v14
	v_cndmask_b32_e64 v9, v9, v15, s[14:15]
	ds_bpermute_b32 v15, v3, v6
	s_waitcnt lgkmcnt(1)
	v_max_i32_e32 v14, v10, v13
	v_min_i32_e32 v10, v10, v13
	s_xor_b64 s[14:15], s[6:7], s[12:13]
	v_cndmask_b32_e64 v10, v10, v14, s[14:15]
	ds_bpermute_b32 v13, v3, v12
	s_waitcnt lgkmcnt(1)
	v_max_i32_e32 v14, v6, v15
	v_min_i32_e32 v6, v6, v15
	v_cndmask_b32_e64 v6, v6, v14, s[14:15]
	ds_bpermute_b32 v14, v3, v9
	s_waitcnt lgkmcnt(1)
	v_max_i32_e32 v15, v12, v13
	v_min_i32_e32 v12, v12, v13
	ds_bpermute_b32 v13, v2, v10
	v_cndmask_b32_e64 v12, v12, v15, s[14:15]
	s_waitcnt lgkmcnt(1)
	v_max_i32_e32 v15, v9, v14
	v_min_i32_e32 v9, v9, v14
	v_cndmask_b32_e64 v9, v9, v15, s[14:15]
	ds_bpermute_b32 v15, v2, v6
	s_waitcnt lgkmcnt(1)
	v_max_i32_e32 v14, v10, v13
	v_min_i32_e32 v10, v10, v13
	s_xor_b64 s[12:13], vcc, s[12:13]
	v_cndmask_b32_e64 v10, v10, v14, s[12:13]
	ds_bpermute_b32 v13, v2, v12
	s_waitcnt lgkmcnt(1)
	v_max_i32_e32 v14, v6, v15
	v_min_i32_e32 v6, v6, v15
	ds_bpermute_b32 v15, v2, v9
	v_cndmask_b32_e64 v6, v6, v14, s[12:13]
	s_waitcnt lgkmcnt(1)
	v_max_i32_e32 v14, v12, v13
	v_min_i32_e32 v12, v12, v13
	v_cndmask_b32_e64 v12, v12, v14, s[12:13]
	s_waitcnt lgkmcnt(0)
	v_max_i32_e32 v13, v9, v15
	v_min_i32_e32 v9, v9, v15
	v_cndmask_b32_e64 v9, v9, v13, s[12:13]
	v_max_i32_e32 v13, v10, v12
	v_min_i32_e32 v10, v10, v12
	v_cmp_eq_u32_e64 s[12:13], 0, v11
	v_max_i32_e32 v12, v6, v9
	v_min_i32_e32 v6, v6, v9
	v_cndmask_b32_e64 v11, v10, v13, s[12:13]
	v_cndmask_b32_e64 v9, v6, v12, s[12:13]
	v_cndmask_b32_e64 v10, v13, v10, s[12:13]
	v_cndmask_b32_e64 v6, v12, v6, s[12:13]
	v_max_i32_e32 v12, v11, v9
	v_min_i32_e32 v9, v11, v9
	v_cndmask_b32_e64 v11, v9, v12, s[12:13]
	v_cndmask_b32_e64 v9, v12, v9, s[12:13]
	v_max_i32_e32 v12, v10, v6
	v_min_i32_e32 v10, v10, v6
	v_xor_b32_e32 v6, 16, v7
	v_cmp_lt_i32_e64 s[14:15], v6, v8
	v_cndmask_b32_e64 v14, v10, v12, s[12:13]
	v_cndmask_b32_e64 v10, v12, v10, s[12:13]
	v_cndmask_b32_e64 v6, v7, v6, s[14:15]
	v_lshlrev_b32_e32 v6, 2, v6
	ds_bpermute_b32 v13, v6, v11
	ds_bpermute_b32 v16, v6, v9
	v_and_b32_e32 v12, 32, v0
	v_cmp_ne_u32_e64 s[14:15], 0, v12
	s_xor_b64 s[16:17], s[12:13], s[14:15]
	s_waitcnt lgkmcnt(1)
	v_max_i32_e32 v15, v11, v13
	v_min_i32_e32 v11, v11, v13
	v_cndmask_b32_e64 v11, v11, v15, s[16:17]
	ds_bpermute_b32 v13, v6, v14
	s_waitcnt lgkmcnt(1)
	v_max_i32_e32 v15, v9, v16
	v_min_i32_e32 v9, v9, v16
	v_cndmask_b32_e64 v9, v9, v15, s[16:17]
	ds_bpermute_b32 v15, v6, v10
	s_waitcnt lgkmcnt(1)
	v_max_i32_e32 v16, v14, v13
	v_min_i32_e32 v13, v14, v13
	ds_bpermute_b32 v14, v5, v11
	v_cndmask_b32_e64 v13, v13, v16, s[16:17]
	s_waitcnt lgkmcnt(1)
	v_max_i32_e32 v16, v10, v15
	v_min_i32_e32 v10, v10, v15
	v_cndmask_b32_e64 v10, v10, v16, s[16:17]
	ds_bpermute_b32 v16, v5, v9
	s_waitcnt lgkmcnt(1)
	v_max_i32_e32 v15, v11, v14
	v_min_i32_e32 v11, v11, v14
	s_xor_b64 s[16:17], s[10:11], s[14:15]
	v_cndmask_b32_e64 v11, v11, v15, s[16:17]
	ds_bpermute_b32 v14, v5, v13
	s_waitcnt lgkmcnt(1)
	v_max_i32_e32 v15, v9, v16
	v_min_i32_e32 v9, v9, v16
	v_cndmask_b32_e64 v9, v9, v15, s[16:17]
	ds_bpermute_b32 v15, v5, v10
	s_waitcnt lgkmcnt(1)
	v_max_i32_e32 v16, v13, v14
	v_min_i32_e32 v13, v13, v14
	ds_bpermute_b32 v14, v4, v11
	v_cndmask_b32_e64 v13, v13, v16, s[16:17]
	s_waitcnt lgkmcnt(1)
	v_max_i32_e32 v16, v10, v15
	v_min_i32_e32 v10, v10, v15
	v_cndmask_b32_e64 v10, v10, v16, s[16:17]
	ds_bpermute_b32 v16, v4, v9
	s_waitcnt lgkmcnt(1)
	v_max_i32_e32 v15, v11, v14
	v_min_i32_e32 v11, v11, v14
	s_xor_b64 s[16:17], s[8:9], s[14:15]
	v_cndmask_b32_e64 v11, v11, v15, s[16:17]
	ds_bpermute_b32 v14, v4, v13
	s_waitcnt lgkmcnt(1)
	v_max_i32_e32 v15, v9, v16
	v_min_i32_e32 v9, v9, v16
	v_cndmask_b32_e64 v9, v9, v15, s[16:17]
	ds_bpermute_b32 v15, v4, v10
	s_waitcnt lgkmcnt(1)
	v_max_i32_e32 v16, v13, v14
	v_min_i32_e32 v13, v13, v14
	ds_bpermute_b32 v14, v3, v11
	v_cndmask_b32_e64 v13, v13, v16, s[16:17]
	s_waitcnt lgkmcnt(1)
	v_max_i32_e32 v16, v10, v15
	v_min_i32_e32 v10, v10, v15
	v_cndmask_b32_e64 v10, v10, v16, s[16:17]
	ds_bpermute_b32 v16, v3, v9
	s_waitcnt lgkmcnt(1)
	v_max_i32_e32 v15, v11, v14
	v_min_i32_e32 v11, v11, v14
	s_xor_b64 s[16:17], s[6:7], s[14:15]
	v_cndmask_b32_e64 v11, v11, v15, s[16:17]
	ds_bpermute_b32 v14, v3, v13
	s_waitcnt lgkmcnt(1)
	v_max_i32_e32 v15, v9, v16
	v_min_i32_e32 v9, v9, v16
	v_cndmask_b32_e64 v9, v9, v15, s[16:17]
	ds_bpermute_b32 v15, v3, v10
	s_waitcnt lgkmcnt(1)
	v_max_i32_e32 v16, v13, v14
	v_min_i32_e32 v13, v13, v14
	ds_bpermute_b32 v14, v2, v11
	v_cndmask_b32_e64 v13, v13, v16, s[16:17]
	s_waitcnt lgkmcnt(1)
	v_max_i32_e32 v16, v10, v15
	v_min_i32_e32 v10, v10, v15
	v_cndmask_b32_e64 v10, v10, v16, s[16:17]
	ds_bpermute_b32 v16, v2, v9
	s_waitcnt lgkmcnt(1)
	v_max_i32_e32 v15, v11, v14
	v_min_i32_e32 v11, v11, v14
	s_xor_b64 s[14:15], vcc, s[14:15]
	v_cndmask_b32_e64 v11, v11, v15, s[14:15]
	ds_bpermute_b32 v14, v2, v13
	s_waitcnt lgkmcnt(1)
	v_max_i32_e32 v15, v9, v16
	v_min_i32_e32 v9, v9, v16
	ds_bpermute_b32 v16, v2, v10
	v_cndmask_b32_e64 v9, v9, v15, s[14:15]
	s_waitcnt lgkmcnt(1)
	v_max_i32_e32 v15, v13, v14
	v_min_i32_e32 v13, v13, v14
	v_cndmask_b32_e64 v13, v13, v15, s[14:15]
	s_waitcnt lgkmcnt(0)
	v_max_i32_e32 v14, v10, v16
	v_min_i32_e32 v10, v10, v16
	v_cndmask_b32_e64 v10, v10, v14, s[14:15]
	v_max_i32_e32 v14, v11, v13
	v_min_i32_e32 v11, v11, v13
	v_cmp_eq_u32_e64 s[14:15], 0, v12
	v_max_i32_e32 v13, v9, v10
	v_min_i32_e32 v9, v9, v10
	v_cndmask_b32_e64 v12, v11, v14, s[14:15]
	v_cndmask_b32_e64 v10, v9, v13, s[14:15]
	v_cndmask_b32_e64 v11, v14, v11, s[14:15]
	v_cndmask_b32_e64 v9, v13, v9, s[14:15]
	v_max_i32_e32 v13, v12, v10
	v_min_i32_e32 v10, v12, v10
	v_cndmask_b32_e64 v12, v10, v13, s[14:15]
	v_cndmask_b32_e64 v10, v13, v10, s[14:15]
	v_max_i32_e32 v13, v11, v9
	v_min_i32_e32 v9, v11, v9
	v_xor_b32_e32 v11, 32, v7
	v_cmp_lt_i32_e64 s[16:17], v11, v8
	v_mov_b32_e32 v251, v197
	s_mov_b32 s31, 0
	v_cndmask_b32_e64 v7, v7, v11, s[16:17]
	v_lshlrev_b32_e32 v7, 2, v7
	ds_bpermute_b32 v8, v7, v12
	ds_bpermute_b32 v15, v7, v10
	v_cndmask_b32_e64 v11, v9, v13, s[14:15]
	v_cndmask_b32_e64 v9, v13, v9, s[14:15]
	v_and_b32_e32 v13, 64, v0
	v_cmp_ne_u32_e64 s[16:17], 0, v13
	s_waitcnt lgkmcnt(1)
	v_max_i32_e32 v14, v12, v8
	v_min_i32_e32 v8, v12, v8
	s_xor_b64 s[18:19], s[14:15], s[16:17]
	v_cndmask_b32_e64 v8, v8, v14, s[18:19]
	ds_bpermute_b32 v12, v7, v11
	s_waitcnt lgkmcnt(1)
	v_max_i32_e32 v14, v10, v15
	v_min_i32_e32 v10, v10, v15
	v_cndmask_b32_e64 v10, v10, v14, s[18:19]
	ds_bpermute_b32 v14, v7, v9
	s_waitcnt lgkmcnt(1)
	v_max_i32_e32 v15, v11, v12
	v_min_i32_e32 v11, v11, v12
	ds_bpermute_b32 v12, v6, v8
	v_cndmask_b32_e64 v11, v11, v15, s[18:19]
	s_waitcnt lgkmcnt(1)
	v_max_i32_e32 v15, v9, v14
	v_min_i32_e32 v9, v9, v14
	v_cndmask_b32_e64 v9, v9, v15, s[18:19]
	ds_bpermute_b32 v15, v6, v10
	s_waitcnt lgkmcnt(1)
	v_max_i32_e32 v14, v8, v12
	v_min_i32_e32 v8, v8, v12
	s_xor_b64 s[18:19], s[12:13], s[16:17]
	v_cndmask_b32_e64 v8, v8, v14, s[18:19]
	ds_bpermute_b32 v12, v6, v11
	s_waitcnt lgkmcnt(1)
	v_max_i32_e32 v14, v10, v15
	v_min_i32_e32 v10, v10, v15
	v_cndmask_b32_e64 v10, v10, v14, s[18:19]
	ds_bpermute_b32 v14, v6, v9
	s_waitcnt lgkmcnt(1)
	v_max_i32_e32 v15, v11, v12
	v_min_i32_e32 v11, v11, v12
	ds_bpermute_b32 v12, v5, v8
	v_cndmask_b32_e64 v11, v11, v15, s[18:19]
	s_waitcnt lgkmcnt(1)
	v_max_i32_e32 v15, v9, v14
	v_min_i32_e32 v9, v9, v14
	v_cndmask_b32_e64 v9, v9, v15, s[18:19]
	ds_bpermute_b32 v15, v5, v10
	s_waitcnt lgkmcnt(1)
	v_max_i32_e32 v14, v8, v12
	v_min_i32_e32 v8, v8, v12
	s_xor_b64 s[18:19], s[10:11], s[16:17]
	v_cndmask_b32_e64 v8, v8, v14, s[18:19]
	ds_bpermute_b32 v12, v5, v11
	s_waitcnt lgkmcnt(1)
	v_max_i32_e32 v14, v10, v15
	v_min_i32_e32 v10, v10, v15
	v_cndmask_b32_e64 v10, v10, v14, s[18:19]
	ds_bpermute_b32 v14, v5, v9
	s_waitcnt lgkmcnt(1)
	v_max_i32_e32 v15, v11, v12
	v_min_i32_e32 v11, v11, v12
	ds_bpermute_b32 v12, v4, v8
	v_cndmask_b32_e64 v11, v11, v15, s[18:19]
	s_waitcnt lgkmcnt(1)
	v_max_i32_e32 v15, v9, v14
	v_min_i32_e32 v9, v9, v14
	v_cndmask_b32_e64 v9, v9, v15, s[18:19]
	ds_bpermute_b32 v15, v4, v10
	s_waitcnt lgkmcnt(1)
	v_max_i32_e32 v14, v8, v12
	v_min_i32_e32 v8, v8, v12
	s_xor_b64 s[18:19], s[8:9], s[16:17]
	v_cndmask_b32_e64 v8, v8, v14, s[18:19]
	ds_bpermute_b32 v12, v4, v11
	s_waitcnt lgkmcnt(1)
	v_max_i32_e32 v14, v10, v15
	v_min_i32_e32 v10, v10, v15
	v_cndmask_b32_e64 v10, v10, v14, s[18:19]
	ds_bpermute_b32 v14, v4, v9
	s_waitcnt lgkmcnt(1)
	v_max_i32_e32 v15, v11, v12
	v_min_i32_e32 v11, v11, v12
	ds_bpermute_b32 v12, v3, v8
	v_cndmask_b32_e64 v11, v11, v15, s[18:19]
	s_waitcnt lgkmcnt(1)
	v_max_i32_e32 v15, v9, v14
	v_min_i32_e32 v9, v9, v14
	v_cndmask_b32_e64 v9, v9, v15, s[18:19]
	ds_bpermute_b32 v15, v3, v10
	s_waitcnt lgkmcnt(1)
	v_max_i32_e32 v14, v8, v12
	v_min_i32_e32 v8, v8, v12
	s_xor_b64 s[18:19], s[6:7], s[16:17]
	v_cndmask_b32_e64 v8, v8, v14, s[18:19]
	ds_bpermute_b32 v12, v3, v11
	s_waitcnt lgkmcnt(1)
	v_max_i32_e32 v14, v10, v15
	v_min_i32_e32 v10, v10, v15
	v_cndmask_b32_e64 v10, v10, v14, s[18:19]
	ds_bpermute_b32 v14, v3, v9
	s_waitcnt lgkmcnt(1)
	v_max_i32_e32 v15, v11, v12
	v_min_i32_e32 v11, v11, v12
	ds_bpermute_b32 v12, v2, v8
	v_cndmask_b32_e64 v11, v11, v15, s[18:19]
	s_waitcnt lgkmcnt(1)
	v_max_i32_e32 v15, v9, v14
	v_min_i32_e32 v9, v9, v14
	v_cndmask_b32_e64 v9, v9, v15, s[18:19]
	ds_bpermute_b32 v15, v2, v10
	s_waitcnt lgkmcnt(1)
	v_max_i32_e32 v14, v8, v12
	v_min_i32_e32 v8, v8, v12
	s_xor_b64 s[16:17], vcc, s[16:17]
	ds_bpermute_b32 v12, v2, v11
	v_cndmask_b32_e64 v8, v8, v14, s[16:17]
	s_waitcnt lgkmcnt(1)
	v_max_i32_e32 v14, v10, v15
	v_min_i32_e32 v10, v10, v15
	ds_bpermute_b32 v15, v2, v9
	v_cndmask_b32_e64 v10, v10, v14, s[16:17]
	s_waitcnt lgkmcnt(1)
	v_max_i32_e32 v14, v11, v12
	v_min_i32_e32 v11, v11, v12
	v_cndmask_b32_e64 v11, v11, v14, s[16:17]
	s_waitcnt lgkmcnt(0)
	v_max_i32_e32 v12, v9, v15
	v_min_i32_e32 v9, v9, v15
	v_cndmask_b32_e64 v9, v9, v12, s[16:17]
	v_max_i32_e32 v12, v8, v11
	v_min_i32_e32 v8, v8, v11
	v_cmp_eq_u32_e64 s[16:17], 0, v13
	v_lshlrev_b32_e32 v208, 11, v82
	v_mov_b32_e32 v209, v197
	v_cndmask_b32_e64 v11, v8, v12, s[16:17]
	v_cndmask_b32_e64 v8, v12, v8, s[16:17]
	v_max_i32_e32 v12, v10, v9
	v_min_i32_e32 v9, v10, v9
	v_cndmask_b32_e64 v10, v9, v12, s[16:17]
	v_cndmask_b32_e64 v9, v12, v9, s[16:17]
	v_max_i32_e32 v13, v11, v10
	v_min_i32_e32 v10, v11, v10
	v_cndmask_b32_e64 v12, v10, v13, s[16:17]
	v_cndmask_b32_e64 v13, v13, v10, s[16:17]
	v_max_i32_e32 v10, v8, v9
	v_min_i32_e32 v8, v8, v9
	v_cndmask_b32_e64 v14, v8, v10, s[16:17]
	v_cndmask_b32_e64 v15, v10, v8, s[16:17]
	ds_write_b128 v1, v[12:15]
	v_xor_b32_e32 v8, 0x100, v252
	s_waitcnt lgkmcnt(0)
	s_barrier
	v_lshl_add_u32 v8, v8, 2, s30
	ds_read_b32 v16, v8
	v_and_b32_e32 v9, 0x80, v0
	v_cmp_ne_u32_e64 s[18:19], 0, v9
	v_xor_b32_e32 v9, 0x101, v252
	v_lshl_add_u32 v9, v9, 2, s30
	v_xor_b32_e32 v10, 0x102, v252
	v_xor_b32_e32 v11, 0x103, v252
	v_lshl_add_u32 v10, v10, 2, s30
	v_lshl_add_u32 v11, v11, 2, s30
	ds_read_b32 v18, v9
	ds_read_b32 v19, v10
	ds_read_b32 v20, v11
	s_waitcnt lgkmcnt(3)
	v_max_i32_e32 v21, v12, v16
	v_min_i32_e32 v12, v12, v16
	s_xor_b64 s[20:21], s[16:17], s[18:19]
	v_cndmask_b32_e64 v12, v12, v21, s[20:21]
	s_waitcnt lgkmcnt(2)
	v_max_i32_e32 v16, v13, v18
	v_min_i32_e32 v13, v13, v18
	v_cndmask_b32_e64 v13, v13, v16, s[20:21]
	ds_bpermute_b32 v18, v7, v12
	s_waitcnt lgkmcnt(2)
	v_max_i32_e32 v16, v14, v19
	v_min_i32_e32 v14, v14, v19
	ds_bpermute_b32 v19, v7, v13
	v_cndmask_b32_e64 v14, v14, v16, s[20:21]
	s_waitcnt lgkmcnt(2)
	v_max_i32_e32 v16, v15, v20
	v_min_i32_e32 v15, v15, v20
	v_cndmask_b32_e64 v15, v15, v16, s[20:21]
	s_waitcnt lgkmcnt(1)
	v_max_i32_e32 v16, v12, v18
	v_min_i32_e32 v12, v12, v18
	s_xor_b64 s[20:21], s[14:15], s[18:19]
	v_cndmask_b32_e64 v12, v12, v16, s[20:21]
	ds_bpermute_b32 v16, v7, v14
	s_waitcnt lgkmcnt(1)
	v_max_i32_e32 v18, v13, v19
	v_min_i32_e32 v13, v13, v19
	v_cndmask_b32_e64 v13, v13, v18, s[20:21]
	ds_bpermute_b32 v18, v7, v15
	s_waitcnt lgkmcnt(1)
	v_max_i32_e32 v19, v14, v16
	v_min_i32_e32 v14, v14, v16
	ds_bpermute_b32 v16, v6, v12
	v_cndmask_b32_e64 v14, v14, v19, s[20:21]
	s_waitcnt lgkmcnt(1)
	v_max_i32_e32 v19, v15, v18
	v_min_i32_e32 v15, v15, v18
	v_cndmask_b32_e64 v15, v15, v19, s[20:21]
	ds_bpermute_b32 v19, v6, v13
	s_waitcnt lgkmcnt(1)
	v_max_i32_e32 v18, v12, v16
	v_min_i32_e32 v12, v12, v16
	s_xor_b64 s[20:21], s[12:13], s[18:19]
	v_cndmask_b32_e64 v12, v12, v18, s[20:21]
	ds_bpermute_b32 v16, v6, v14
	s_waitcnt lgkmcnt(1)
	v_max_i32_e32 v18, v13, v19
	v_min_i32_e32 v13, v13, v19
	v_cndmask_b32_e64 v13, v13, v18, s[20:21]
	ds_bpermute_b32 v18, v6, v15
	s_waitcnt lgkmcnt(1)
	v_max_i32_e32 v19, v14, v16
	v_min_i32_e32 v14, v14, v16
	ds_bpermute_b32 v16, v5, v12
	v_cndmask_b32_e64 v14, v14, v19, s[20:21]
	s_waitcnt lgkmcnt(1)
	v_max_i32_e32 v19, v15, v18
	v_min_i32_e32 v15, v15, v18
	v_cndmask_b32_e64 v15, v15, v19, s[20:21]
	ds_bpermute_b32 v19, v5, v13
	s_waitcnt lgkmcnt(1)
	v_max_i32_e32 v18, v12, v16
	v_min_i32_e32 v12, v12, v16
	s_xor_b64 s[20:21], s[10:11], s[18:19]
	v_cndmask_b32_e64 v12, v12, v18, s[20:21]
	ds_bpermute_b32 v16, v5, v14
	s_waitcnt lgkmcnt(1)
	v_max_i32_e32 v18, v13, v19
	v_min_i32_e32 v13, v13, v19
	v_cndmask_b32_e64 v13, v13, v18, s[20:21]
	ds_bpermute_b32 v18, v5, v15
	s_waitcnt lgkmcnt(1)
	v_max_i32_e32 v19, v14, v16
	v_min_i32_e32 v14, v14, v16
	ds_bpermute_b32 v16, v4, v12
	v_cndmask_b32_e64 v14, v14, v19, s[20:21]
	s_waitcnt lgkmcnt(1)
	v_max_i32_e32 v19, v15, v18
	v_min_i32_e32 v15, v15, v18
	v_cndmask_b32_e64 v15, v15, v19, s[20:21]
	ds_bpermute_b32 v19, v4, v13
	s_waitcnt lgkmcnt(1)
	v_max_i32_e32 v18, v12, v16
	v_min_i32_e32 v12, v12, v16
	s_xor_b64 s[20:21], s[8:9], s[18:19]
	v_cndmask_b32_e64 v12, v12, v18, s[20:21]
	ds_bpermute_b32 v16, v4, v14
	s_waitcnt lgkmcnt(1)
	v_max_i32_e32 v18, v13, v19
	v_min_i32_e32 v13, v13, v19
	v_cndmask_b32_e64 v13, v13, v18, s[20:21]
	ds_bpermute_b32 v18, v4, v15
	s_waitcnt lgkmcnt(1)
	v_max_i32_e32 v19, v14, v16
	v_min_i32_e32 v14, v14, v16
	ds_bpermute_b32 v16, v3, v12
	v_cndmask_b32_e64 v14, v14, v19, s[20:21]
	s_waitcnt lgkmcnt(1)
	v_max_i32_e32 v19, v15, v18
	v_min_i32_e32 v15, v15, v18
	v_cndmask_b32_e64 v15, v15, v19, s[20:21]
	ds_bpermute_b32 v19, v3, v13
	s_waitcnt lgkmcnt(1)
	v_max_i32_e32 v18, v12, v16
	v_min_i32_e32 v12, v12, v16
	s_xor_b64 s[20:21], s[6:7], s[18:19]
	v_cndmask_b32_e64 v12, v12, v18, s[20:21]
	ds_bpermute_b32 v16, v3, v14
	s_waitcnt lgkmcnt(1)
	v_max_i32_e32 v18, v13, v19
	v_min_i32_e32 v13, v13, v19
	v_cndmask_b32_e64 v13, v13, v18, s[20:21]
	ds_bpermute_b32 v18, v3, v15
	s_waitcnt lgkmcnt(1)
	v_max_i32_e32 v19, v14, v16
	v_min_i32_e32 v14, v14, v16
	ds_bpermute_b32 v16, v2, v12
	v_cndmask_b32_e64 v14, v14, v19, s[20:21]
	s_waitcnt lgkmcnt(1)
	v_max_i32_e32 v19, v15, v18
	v_min_i32_e32 v15, v15, v18
	v_cndmask_b32_e64 v15, v15, v19, s[20:21]
	ds_bpermute_b32 v19, v2, v13
	s_waitcnt lgkmcnt(1)
	v_max_i32_e32 v18, v12, v16
	v_min_i32_e32 v12, v12, v16
	s_xor_b64 s[18:19], vcc, s[18:19]
	ds_bpermute_b32 v16, v2, v14
	v_cndmask_b32_e64 v12, v12, v18, s[18:19]
	s_waitcnt lgkmcnt(1)
	v_max_i32_e32 v18, v13, v19
	v_min_i32_e32 v13, v13, v19
	ds_bpermute_b32 v19, v2, v15
	v_cndmask_b32_e64 v13, v13, v18, s[18:19]
	s_waitcnt lgkmcnt(1)
	v_max_i32_e32 v18, v14, v16
	v_min_i32_e32 v14, v14, v16
	v_cndmask_b32_e64 v14, v14, v18, s[18:19]
	s_waitcnt lgkmcnt(0)
	v_max_i32_e32 v16, v15, v19
	v_min_i32_e32 v15, v15, v19
	v_cndmask_b32_e64 v15, v15, v16, s[18:19]
	v_max_i32_e32 v16, v12, v14
	v_min_i32_e32 v12, v12, v14
	v_cmp_eq_u32_e64 s[18:19], 0, v17
	s_waitcnt lgkmcnt(0)
	s_barrier
	v_and_b32_e32 v18, 0x100, v0
	v_cmp_ne_u32_e64 s[20:21], 0, v18
	v_cndmask_b32_e64 v14, v12, v16, s[18:19]
	v_cndmask_b32_e64 v16, v16, v12, s[18:19]
	v_max_i32_e32 v12, v13, v15
	v_min_i32_e32 v13, v13, v15
	v_cndmask_b32_e64 v15, v13, v12, s[18:19]
	v_cndmask_b32_e64 v17, v12, v13, s[18:19]
	v_max_i32_e32 v13, v14, v15
	v_min_i32_e32 v14, v14, v15
	v_max_i32_e32 v15, v16, v17
	v_min_i32_e32 v16, v16, v17
	v_cndmask_b32_e64 v12, v14, v13, s[18:19]
	v_cndmask_b32_e64 v13, v13, v14, s[18:19]
	v_cndmask_b32_e64 v14, v16, v15, s[18:19]
	v_cndmask_b32_e64 v15, v15, v16, s[18:19]
	ds_write_b128 v1, v[12:15]
	v_xor_b32_e32 v16, 0x200, v252
	s_waitcnt lgkmcnt(0)
	s_barrier
	v_lshl_add_u32 v16, v16, 2, s30
	ds_read_b32 v17, v16
	v_xor_b32_e32 v18, 0x201, v252
	v_lshl_add_u32 v18, v18, 2, s30
	v_xor_b32_e32 v19, 0x202, v252
	v_xor_b32_e32 v20, 0x203, v252
	v_lshl_add_u32 v19, v19, 2, s30
	v_lshl_add_u32 v20, v20, 2, s30
	ds_read_b32 v21, v18
	ds_read_b32 v22, v19
	ds_read_b32 v23, v20
	s_waitcnt lgkmcnt(3)
	v_max_i32_e32 v24, v12, v17
	v_min_i32_e32 v12, v12, v17
	s_xor_b64 s[22:23], s[18:19], s[20:21]
	s_waitcnt lgkmcnt(2)
	v_max_i32_e32 v17, v13, v21
	v_min_i32_e32 v13, v13, v21
	v_cndmask_b32_e64 v13, v13, v17, s[22:23]
	s_waitcnt lgkmcnt(1)
	v_max_i32_e32 v17, v14, v22
	v_min_i32_e32 v14, v14, v22
	v_cndmask_b32_e64 v14, v14, v17, s[22:23]
	s_waitcnt lgkmcnt(0)
	v_max_i32_e32 v17, v15, v23
	v_min_i32_e32 v15, v15, v23
	v_cndmask_b32_e64 v12, v12, v24, s[22:23]
	v_cndmask_b32_e64 v15, v15, v17, s[22:23]
	s_waitcnt lgkmcnt(0)
	s_barrier
	ds_write_b128 v1, v[12:15]
	s_waitcnt lgkmcnt(0)
	s_barrier
	ds_read_b32 v17, v8
	ds_read_b32 v22, v9
	ds_read_b32 v23, v10
	ds_read_b32 v24, v11
	s_xor_b64 s[22:23], s[16:17], s[20:21]
	v_and_b32_e32 v21, 0x100, v0
	s_waitcnt lgkmcnt(0)
	s_barrier
	s_waitcnt lgkmcnt(3)
	v_max_i32_e32 v25, v12, v17
	v_min_i32_e32 v12, v12, v17
	v_cndmask_b32_e64 v12, v12, v25, s[22:23]
	s_waitcnt lgkmcnt(2)
	v_max_i32_e32 v17, v13, v22
	v_min_i32_e32 v13, v13, v22
	v_cndmask_b32_e64 v13, v13, v17, s[22:23]
	ds_bpermute_b32 v22, v7, v12
	s_waitcnt lgkmcnt(2)
	v_max_i32_e32 v17, v14, v23
	v_min_i32_e32 v14, v14, v23
	ds_bpermute_b32 v23, v7, v13
	v_cndmask_b32_e64 v14, v14, v17, s[22:23]
	s_waitcnt lgkmcnt(2)
	v_max_i32_e32 v17, v15, v24
	v_min_i32_e32 v15, v15, v24
	v_cndmask_b32_e64 v15, v15, v17, s[22:23]
	s_waitcnt lgkmcnt(1)
	v_max_i32_e32 v17, v12, v22
	v_min_i32_e32 v12, v12, v22
	s_xor_b64 s[22:23], s[14:15], s[20:21]
	v_cndmask_b32_e64 v12, v12, v17, s[22:23]
	ds_bpermute_b32 v17, v7, v14
	s_waitcnt lgkmcnt(1)
	v_max_i32_e32 v22, v13, v23
	v_min_i32_e32 v13, v13, v23
	v_cndmask_b32_e64 v13, v13, v22, s[22:23]
	ds_bpermute_b32 v22, v7, v15
	s_waitcnt lgkmcnt(1)
	v_max_i32_e32 v23, v14, v17
	v_min_i32_e32 v14, v14, v17
	ds_bpermute_b32 v17, v6, v12
	v_cndmask_b32_e64 v14, v14, v23, s[22:23]
	s_waitcnt lgkmcnt(1)
	v_max_i32_e32 v23, v15, v22
	v_min_i32_e32 v15, v15, v22
	v_cndmask_b32_e64 v15, v15, v23, s[22:23]
	ds_bpermute_b32 v23, v6, v13
	s_waitcnt lgkmcnt(1)
	v_max_i32_e32 v22, v12, v17
	v_min_i32_e32 v12, v12, v17
	s_xor_b64 s[22:23], s[12:13], s[20:21]
	v_cndmask_b32_e64 v12, v12, v22, s[22:23]
	ds_bpermute_b32 v17, v6, v14
	s_waitcnt lgkmcnt(1)
	v_max_i32_e32 v22, v13, v23
	v_min_i32_e32 v13, v13, v23
	v_cndmask_b32_e64 v13, v13, v22, s[22:23]
	ds_bpermute_b32 v22, v6, v15
	s_waitcnt lgkmcnt(1)
	v_max_i32_e32 v23, v14, v17
	v_min_i32_e32 v14, v14, v17
	ds_bpermute_b32 v17, v5, v12
	v_cndmask_b32_e64 v14, v14, v23, s[22:23]
	s_waitcnt lgkmcnt(1)
	v_max_i32_e32 v23, v15, v22
	v_min_i32_e32 v15, v15, v22
	v_cndmask_b32_e64 v15, v15, v23, s[22:23]
	ds_bpermute_b32 v23, v5, v13
	s_waitcnt lgkmcnt(1)
	v_max_i32_e32 v22, v12, v17
	v_min_i32_e32 v12, v12, v17
	s_xor_b64 s[22:23], s[10:11], s[20:21]
	v_cndmask_b32_e64 v12, v12, v22, s[22:23]
	ds_bpermute_b32 v17, v5, v14
	s_waitcnt lgkmcnt(1)
	v_max_i32_e32 v22, v13, v23
	v_min_i32_e32 v13, v13, v23
	v_cndmask_b32_e64 v13, v13, v22, s[22:23]
	ds_bpermute_b32 v22, v5, v15
	s_waitcnt lgkmcnt(1)
	v_max_i32_e32 v23, v14, v17
	v_min_i32_e32 v14, v14, v17
	ds_bpermute_b32 v17, v4, v12
	v_cndmask_b32_e64 v14, v14, v23, s[22:23]
	s_waitcnt lgkmcnt(1)
	v_max_i32_e32 v23, v15, v22
	v_min_i32_e32 v15, v15, v22
	v_cndmask_b32_e64 v15, v15, v23, s[22:23]
	ds_bpermute_b32 v23, v4, v13
	s_waitcnt lgkmcnt(1)
	v_max_i32_e32 v22, v12, v17
	v_min_i32_e32 v12, v12, v17
	s_xor_b64 s[22:23], s[8:9], s[20:21]
	v_cndmask_b32_e64 v12, v12, v22, s[22:23]
	ds_bpermute_b32 v17, v4, v14
	s_waitcnt lgkmcnt(1)
	v_max_i32_e32 v22, v13, v23
	v_min_i32_e32 v13, v13, v23
	v_cndmask_b32_e64 v13, v13, v22, s[22:23]
	ds_bpermute_b32 v22, v4, v15
	s_waitcnt lgkmcnt(1)
	v_max_i32_e32 v23, v14, v17
	v_min_i32_e32 v14, v14, v17
	ds_bpermute_b32 v17, v3, v12
	v_cndmask_b32_e64 v14, v14, v23, s[22:23]
	s_waitcnt lgkmcnt(1)
	v_max_i32_e32 v23, v15, v22
	v_min_i32_e32 v15, v15, v22
	v_cndmask_b32_e64 v15, v15, v23, s[22:23]
	ds_bpermute_b32 v23, v3, v13
	s_waitcnt lgkmcnt(1)
	v_max_i32_e32 v22, v12, v17
	v_min_i32_e32 v12, v12, v17
	s_xor_b64 s[22:23], s[6:7], s[20:21]
	v_cndmask_b32_e64 v12, v12, v22, s[22:23]
	ds_bpermute_b32 v17, v3, v14
	s_waitcnt lgkmcnt(1)
	v_max_i32_e32 v22, v13, v23
	v_min_i32_e32 v13, v13, v23
	v_cndmask_b32_e64 v13, v13, v22, s[22:23]
	ds_bpermute_b32 v22, v3, v15
	s_waitcnt lgkmcnt(1)
	v_max_i32_e32 v23, v14, v17
	v_min_i32_e32 v14, v14, v17
	ds_bpermute_b32 v17, v2, v12
	v_cndmask_b32_e64 v14, v14, v23, s[22:23]
	s_waitcnt lgkmcnt(1)
	v_max_i32_e32 v23, v15, v22
	v_min_i32_e32 v15, v15, v22
	v_cndmask_b32_e64 v15, v15, v23, s[22:23]
	ds_bpermute_b32 v23, v2, v13
	s_waitcnt lgkmcnt(1)
	v_max_i32_e32 v22, v12, v17
	v_min_i32_e32 v12, v12, v17
	s_xor_b64 s[20:21], vcc, s[20:21]
	ds_bpermute_b32 v17, v2, v14
	v_cndmask_b32_e64 v12, v12, v22, s[20:21]
	s_waitcnt lgkmcnt(1)
	v_max_i32_e32 v22, v13, v23
	v_min_i32_e32 v13, v13, v23
	ds_bpermute_b32 v23, v2, v15
	v_cndmask_b32_e64 v13, v13, v22, s[20:21]
	s_waitcnt lgkmcnt(1)
	v_max_i32_e32 v22, v14, v17
	v_min_i32_e32 v14, v14, v17
	v_cndmask_b32_e64 v14, v14, v22, s[20:21]
	s_waitcnt lgkmcnt(0)
	v_max_i32_e32 v17, v15, v23
	v_min_i32_e32 v15, v15, v23
	v_cndmask_b32_e64 v15, v15, v17, s[20:21]
	v_max_i32_e32 v17, v12, v14
	v_min_i32_e32 v12, v12, v14
	v_cmp_eq_u32_e64 s[22:23], 0, v21
	v_xor_b32_e32 v22, 0x402, v252
	v_xor_b32_e32 v23, 0x403, v252
	v_cndmask_b32_e64 v14, v12, v17, s[22:23]
	v_cndmask_b32_e64 v17, v17, v12, s[22:23]
	v_max_i32_e32 v12, v13, v15
	v_min_i32_e32 v13, v13, v15
	v_cndmask_b32_e64 v15, v13, v12, s[22:23]
	v_cndmask_b32_e64 v21, v12, v13, s[22:23]
	v_max_i32_e32 v13, v14, v15
	v_min_i32_e32 v14, v14, v15
	v_max_i32_e32 v15, v17, v21
	v_min_i32_e32 v17, v17, v21
	v_cndmask_b32_e64 v12, v14, v13, s[22:23]
	v_cndmask_b32_e64 v13, v13, v14, s[22:23]
	v_cndmask_b32_e64 v14, v17, v15, s[22:23]
	v_cndmask_b32_e64 v15, v15, v17, s[22:23]
	ds_write_b128 v1, v[12:15]
	v_xor_b32_e32 v17, 0x400, v252
	s_waitcnt lgkmcnt(0)
	s_barrier
	v_lshl_add_u32 v17, v17, 2, s30
	ds_read_b32 v17, v17
	v_xor_b32_e32 v21, 0x401, v252
	v_lshl_add_u32 v21, v21, 2, s30
	v_lshl_add_u32 v22, v22, 2, s30
	v_lshl_add_u32 v23, v23, 2, s30
	ds_read_b32 v21, v21
	ds_read_b32 v22, v22
	ds_read_b32 v23, v23
	s_movk_i32 s20, 0x1ff
	v_cmp_lt_u32_e64 s[20:21], s20, v0
	s_waitcnt lgkmcnt(3)
	v_max_i32_e32 v24, v12, v17
	v_min_i32_e32 v12, v12, v17
	s_xor_b64 s[22:23], s[22:23], s[20:21]
	s_waitcnt lgkmcnt(2)
	v_max_i32_e32 v17, v13, v21
	v_min_i32_e32 v13, v13, v21
	v_cndmask_b32_e64 v13, v13, v17, s[22:23]
	s_waitcnt lgkmcnt(1)
	v_max_i32_e32 v17, v14, v22
	v_min_i32_e32 v14, v14, v22
	v_cndmask_b32_e64 v14, v14, v17, s[22:23]
	s_waitcnt lgkmcnt(0)
	v_max_i32_e32 v17, v15, v23
	v_min_i32_e32 v15, v15, v23
	v_cndmask_b32_e64 v12, v12, v24, s[22:23]
	v_cndmask_b32_e64 v15, v15, v17, s[22:23]
	s_waitcnt lgkmcnt(0)
	s_barrier
	ds_write_b128 v1, v[12:15]
	s_waitcnt lgkmcnt(0)
	s_barrier
	ds_read_b32 v16, v16
	ds_read_b32 v17, v18
	ds_read_b32 v18, v19
	ds_read_b32 v19, v20
	s_xor_b64 s[18:19], s[18:19], s[20:21]
	s_waitcnt lgkmcnt(0)
	s_barrier
	s_xor_b64 s[16:17], s[16:17], s[20:21]
	s_waitcnt lgkmcnt(3)
	v_max_i32_e32 v20, v12, v16
	v_min_i32_e32 v12, v12, v16
	s_waitcnt lgkmcnt(2)
	v_max_i32_e32 v16, v13, v17
	v_min_i32_e32 v13, v13, v17
	v_cndmask_b32_e64 v13, v13, v16, s[18:19]
	s_waitcnt lgkmcnt(1)
	v_max_i32_e32 v16, v14, v18
	v_min_i32_e32 v14, v14, v18
	v_cndmask_b32_e64 v14, v14, v16, s[18:19]
	s_waitcnt lgkmcnt(0)
	v_max_i32_e32 v16, v15, v19
	v_min_i32_e32 v15, v15, v19
	v_cndmask_b32_e64 v12, v12, v20, s[18:19]
	v_cndmask_b32_e64 v15, v15, v16, s[18:19]
	ds_write_b128 v1, v[12:15]
	s_waitcnt lgkmcnt(0)
	s_barrier
	ds_read_b32 v8, v8
	ds_read_b32 v9, v9
	ds_read_b32 v10, v10
	ds_read_b32 v11, v11
	s_xor_b64 s[14:15], s[14:15], s[20:21]
	s_xor_b64 s[12:13], s[12:13], s[20:21]
	s_xor_b64 s[10:11], s[10:11], s[20:21]
	s_waitcnt lgkmcnt(3)
	v_max_i32_e32 v16, v12, v8
	v_min_i32_e32 v8, v12, v8
	v_cndmask_b32_e64 v8, v8, v16, s[16:17]
	s_waitcnt lgkmcnt(2)
	v_max_i32_e32 v12, v13, v9
	v_min_i32_e32 v9, v13, v9
	ds_bpermute_b32 v13, v7, v8
	v_cndmask_b32_e64 v9, v9, v12, s[16:17]
	s_waitcnt lgkmcnt(2)
	v_max_i32_e32 v12, v14, v10
	v_min_i32_e32 v10, v14, v10
	v_cndmask_b32_e64 v10, v10, v12, s[16:17]
	s_waitcnt lgkmcnt(1)
	v_max_i32_e32 v12, v15, v11
	v_min_i32_e32 v11, v15, v11
	v_cndmask_b32_e64 v11, v11, v12, s[16:17]
	s_waitcnt lgkmcnt(0)
	v_max_i32_e32 v12, v8, v13
	ds_bpermute_b32 v14, v7, v9
	v_min_i32_e32 v8, v8, v13
	v_cndmask_b32_e64 v8, v8, v12, s[14:15]
	ds_bpermute_b32 v12, v7, v10
	ds_bpermute_b32 v7, v7, v11
	s_waitcnt lgkmcnt(2)
	v_max_i32_e32 v13, v9, v14
	v_min_i32_e32 v9, v9, v14
	v_cndmask_b32_e64 v9, v9, v13, s[14:15]
	s_waitcnt lgkmcnt(1)
	v_max_i32_e32 v13, v10, v12
	v_min_i32_e32 v10, v10, v12
	ds_bpermute_b32 v12, v6, v8
	v_cndmask_b32_e64 v10, v10, v13, s[14:15]
	s_waitcnt lgkmcnt(1)
	v_max_i32_e32 v13, v11, v7
	v_min_i32_e32 v7, v11, v7
	v_cndmask_b32_e64 v7, v7, v13, s[14:15]
	s_waitcnt lgkmcnt(0)
	v_max_i32_e32 v11, v8, v12
	ds_bpermute_b32 v13, v6, v9
	v_min_i32_e32 v8, v8, v12
	v_cndmask_b32_e64 v8, v8, v11, s[12:13]
	ds_bpermute_b32 v11, v6, v10
	ds_bpermute_b32 v6, v6, v7
	s_waitcnt lgkmcnt(2)
	v_max_i32_e32 v12, v9, v13
	v_min_i32_e32 v9, v9, v13
	v_cndmask_b32_e64 v9, v9, v12, s[12:13]
	s_waitcnt lgkmcnt(1)
	v_max_i32_e32 v12, v10, v11
	v_min_i32_e32 v10, v10, v11
	ds_bpermute_b32 v11, v5, v8
	v_cndmask_b32_e64 v10, v10, v12, s[12:13]
	s_waitcnt lgkmcnt(1)
	v_max_i32_e32 v12, v7, v6
	v_min_i32_e32 v6, v7, v6
	v_cndmask_b32_e64 v6, v6, v12, s[12:13]
	s_waitcnt lgkmcnt(0)
	v_max_i32_e32 v7, v8, v11
	ds_bpermute_b32 v12, v5, v9
	v_min_i32_e32 v8, v8, v11
	v_cndmask_b32_e64 v7, v8, v7, s[10:11]
	ds_bpermute_b32 v8, v5, v10
	ds_bpermute_b32 v5, v5, v6
	s_waitcnt lgkmcnt(2)
	v_max_i32_e32 v11, v9, v12
	v_min_i32_e32 v9, v9, v12
	v_cndmask_b32_e64 v9, v9, v11, s[10:11]
	s_waitcnt lgkmcnt(1)
	v_max_i32_e32 v11, v10, v8
	v_min_i32_e32 v8, v10, v8
	ds_bpermute_b32 v10, v4, v7
	v_cndmask_b32_e64 v8, v8, v11, s[10:11]
	s_waitcnt lgkmcnt(1)
	v_max_i32_e32 v11, v6, v5
	v_min_i32_e32 v5, v6, v5
	v_cndmask_b32_e64 v5, v5, v11, s[10:11]
	s_waitcnt lgkmcnt(0)
	v_max_i32_e32 v6, v7, v10
	ds_bpermute_b32 v11, v4, v9
	v_min_i32_e32 v7, v7, v10
	s_xor_b64 s[8:9], s[8:9], s[20:21]
	v_cndmask_b32_e64 v6, v7, v6, s[8:9]
	ds_bpermute_b32 v7, v4, v8
	s_waitcnt lgkmcnt(1)
	v_max_i32_e32 v10, v9, v11
	v_min_i32_e32 v9, v9, v11
	ds_bpermute_b32 v4, v4, v5
	v_cndmask_b32_e64 v9, v9, v10, s[8:9]
	s_waitcnt lgkmcnt(1)
	v_max_i32_e32 v10, v8, v7
	v_min_i32_e32 v7, v8, v7
	ds_bpermute_b32 v8, v3, v6
	v_cndmask_b32_e64 v7, v7, v10, s[8:9]
	s_waitcnt lgkmcnt(1)
	v_max_i32_e32 v10, v5, v4
	v_min_i32_e32 v4, v5, v4
	v_cndmask_b32_e64 v4, v4, v10, s[8:9]
	s_waitcnt lgkmcnt(0)
	v_max_i32_e32 v5, v6, v8
	ds_bpermute_b32 v10, v3, v9
	v_min_i32_e32 v6, v6, v8
	s_xor_b64 s[6:7], s[6:7], s[20:21]
	v_cndmask_b32_e64 v5, v6, v5, s[6:7]
	ds_bpermute_b32 v6, v3, v7
	s_waitcnt lgkmcnt(1)
	v_max_i32_e32 v8, v9, v10
	v_min_i32_e32 v9, v9, v10
	ds_bpermute_b32 v3, v3, v4
	v_cndmask_b32_e64 v8, v9, v8, s[6:7]
	s_waitcnt lgkmcnt(1)
	v_max_i32_e32 v9, v7, v6
	v_min_i32_e32 v6, v7, v6
	ds_bpermute_b32 v7, v2, v5
	v_cndmask_b32_e64 v6, v6, v9, s[6:7]
	s_waitcnt lgkmcnt(1)
	v_max_i32_e32 v9, v4, v3
	v_min_i32_e32 v3, v4, v3
	v_cndmask_b32_e64 v3, v3, v9, s[6:7]
	s_waitcnt lgkmcnt(0)
	v_max_i32_e32 v4, v5, v7
	ds_bpermute_b32 v9, v2, v8
	v_min_i32_e32 v5, v5, v7
	s_xor_b64 vcc, vcc, s[20:21]
	v_cndmask_b32_e32 v4, v5, v4, vcc
	ds_bpermute_b32 v5, v2, v6
	ds_bpermute_b32 v2, v2, v3
	s_waitcnt lgkmcnt(2)
	v_max_i32_e32 v7, v8, v9
	v_min_i32_e32 v8, v8, v9
	v_cndmask_b32_e32 v7, v8, v7, vcc
	s_waitcnt lgkmcnt(1)
	v_max_i32_e32 v8, v6, v5
	v_min_i32_e32 v5, v6, v5
	s_movk_i32 s18, 0x200
	v_cndmask_b32_e32 v5, v5, v8, vcc
	s_waitcnt lgkmcnt(0)
	v_max_i32_e32 v6, v3, v2
	v_min_i32_e32 v2, v3, v2
	v_cndmask_b32_e32 v2, v2, v6, vcc
	v_max_i32_e32 v3, v4, v5
	v_min_i32_e32 v4, v4, v5
	v_cmp_gt_u32_e32 vcc, s18, v0
	s_add_i32 s8, 0, 0x20100
	s_cmp_lg_u32 0, -1
	v_cndmask_b32_e32 v5, v4, v3, vcc
	v_cndmask_b32_e32 v4, v3, v4, vcc
	v_max_i32_e32 v3, v7, v2
	v_min_i32_e32 v2, v7, v2
	v_cndmask_b32_e32 v6, v2, v3, vcc
	v_cndmask_b32_e32 v7, v3, v2, vcc
	v_max_i32_e32 v3, v5, v6
	v_min_i32_e32 v5, v5, v6
	v_cndmask_b32_e32 v2, v5, v3, vcc
	v_cndmask_b32_e32 v3, v3, v5, vcc
	v_max_i32_e32 v5, v4, v7
	v_min_i32_e32 v6, v4, v7
	v_cndmask_b32_e32 v4, v6, v5, vcc
	v_cndmask_b32_e32 v5, v5, v6, vcc
	s_waitcnt lgkmcnt(0)
	s_barrier
	ds_write_b128 v1, v[2:5]
	v_lshl_add_u32 v230, v0, 2, s8
	v_lshrrev_b32_e32 v3, 5, v82
	s_cselect_b32 s8, 0, 0
	v_and_b32_e32 v1, 32, v193
	s_addk_i32 s8, 0x6000
	v_lshlrev_b32_e32 v231, 2, v3
	v_lshrrev_b32_e32 v4, 2, v0
	v_add_u32_e32 v5, s8, v1
	v_and_or_b32 v4, v4, 3, v231
	v_add_u32_e32 v9, 0, v1
	v_lshlrev_b32_e32 v1, 10, v205
	s_movk_i32 s22, 0x100
	v_and_b32_e32 v2, 24, v158
	v_lshlrev_b32_e32 v6, 6, v4
	v_lshlrev_b32_e32 v7, 10, v3
	v_lshl_or_b32 v4, v3, 3, v1
	s_add_i32 s8, 0, 0x15000
	v_lshlrev_b32_e32 v1, 4, v3
	v_lshlrev_b32_e32 v207, 9, v3
	v_lshrrev_b32_e32 v3, 3, v82
	v_cmp_gt_u32_e64 s[6:7], s22, v0
	v_add_u32_e32 v233, s8, v1
	v_add3_u32 v234, v5, v2, v6
	v_or_b32_e32 v5, 8, v3
	v_add_u32_e32 v236, s8, v250
	v_readlane_b32 s8, v253, 46
	v_lshlrev_b32_e32 v8, 4, v205
	v_lshlrev_b32_e32 v195, 7, v3
	v_lshlrev_b32_e32 v200, 10, v3
	v_lshlrev_b32_e32 v199, 7, v5
	v_lshlrev_b32_e32 v202, 10, v5
	v_or_b32_e32 v5, 16, v3
	v_or_b32_e32 v3, 24, v3
	v_readlane_b32 s9, v253, 47
	v_readlane_b32 s20, v253, 58
	v_readlane_b32 s21, v253, 59
	v_readlane_b32 s22, v253, 60
	v_readlane_b32 s23, v253, 61
	v_add3_u32 v232, 0, v7, v8
	v_add3_u32 v235, v9, v2, v6
	v_lshlrev_b32_e32 v203, 7, v3
	v_lshlrev_b32_e32 v206, 10, v3
	v_readlane_b32 s10, v253, 48
	v_readlane_b32 s11, v253, 49
	v_readlane_b32 s12, v253, 50
	v_readlane_b32 s13, v253, 51
	v_readlane_b32 s14, v253, 52
	v_readlane_b32 s15, v253, 53
	v_readlane_b32 s16, v253, 54
	v_readlane_b32 s17, v253, 55
	v_readlane_b32 s18, v253, 56
	v_readlane_b32 s19, v253, 57
	v_lshl_add_u64 v[6:7], s[22:23], 0, v[250:251]
	s_mov_b64 s[8:9], 0x1480000
	v_add_u32_e32 v3, 0, v1
	s_mov_b32 s20, 0xfffe0000
	v_and_b32_e32 v198, 56, v158
	v_lshlrev_b32_e32 v201, 7, v5
	v_lshlrev_b32_e32 v204, 10, v5
	v_lshl_add_u64 v[210:211], v[6:7], 0, s[8:9]
	v_add_u32_e32 v241, 0x15100, v3
	v_or_b32_e32 v237, 0x17b, v231
	s_mov_b64 s[10:11], 0x2000
	v_lshlrev_b32_e32 v212, 1, v2
	s_mov_b64 s[12:13], 0x20000
	v_lshlrev_b32_e32 v238, 1, v4
	s_mov_b64 s[14:15], 0x40000
	s_mov_b64 s[16:17], 0x60000
	s_mov_b64 s[18:19], 0xa0000
	s_mov_b32 s21, -1
	s_mov_b64 s[22:23], 0x80000
	s_movk_i32 s46, 0x1000
	v_mov_b32_e32 v239, 0x7f800000
	v_mov_b32_e32 v240, 0xff800000
	s_mov_b32 s47, 0
	s_cmp_lg_u32 s92, 0
	s_cbranch_scc1 .Lgw_end_9
	s_mov_b64 exec, 1
	v_mov_b32_e32 v2, 0x22160
	ds_read_b32 v246, v2
	s_lshr_b32 s8, s99, 16
	s_add_u32 s8, s100, s8
	s_addc_u32 s9, s101, 0
	s_min_u32 s30, s98, 8
	v_mov_b32_e32 v2, 0
	v_mov_b32_e32 v247, 0
	s_waitcnt lgkmcnt(0)
	v_readfirstlane_b32 vcc_lo, v246
	s_mul_i32 s30, s30, vcc_lo

.Lgw_end_9x:
	s_mov_b64 exec, -1
